# P7 epilogue: residual-row ring 9 deep instead of 7 (v176..v247)
# baseline (speedup 1.0000x reference)
; __device__ __forceinline__ unsigned cvt_pk_bf16(float lo, float hi) { unsigned r; asm volatile("v_cvt_pk_bf16_f32 %0, %1, %2" : "=v"(r) : "v"(lo), "v"(hi)); return r; }
; __device__ __forceinline__ unsigned cvt_pk4_fp8(float a, float b, float c, float d) { int w; asm("" : "=v"(w));     w = __builtin_amdgcn_cvt_pk_fp8_f32(a, b, w, false); w = __builtin_amdgcn_cvt_pk_fp8_f32(c, d, w, true); return (unsigned)w; }
;     __device__ __forceinline__ void operator()(const f32x4 (&acc)[2][2][4][2], const Unit& u, int wr, int wc, int fr, int fq) const {
;         const int row0 = u.pm * BM + wr * 64 + fr, col0 = u.pn * BM + wc * 32 + 8 * fq;
;         f32x4 gv[2][2];
; #pragma unroll
;         for (int bj = 0; bj < 2; ++bj)
; #pragma unroll
;             for (int n = 0; n < 2; ++n) gv[bj][n] = *(const f32x4*)(g + col0 + bj * HALF + 4 * n);
; #pragma unroll
;         for (int ai = 0; ai < 2; ++ai)
; #pragma unroll
;             for (int m = 0; m < 4; ++m) { const size_t off = (size_t)(row0 + ai * HALF + m * 16) * DM + col0;
; #pragma unroll
;                 for (int bj = 0; bj < 2; ++bj) { const f32x4 v0 = *(const f32x4*)(base + off + bj * HALF) + acc[ai][bj][m][0], v1 = *(const f32x4*)(base + off + bj * HALF + 4) + acc[ai][bj][m][1];
;                     { u32x4 xw; xw.x = cvt_pk_bf16(v0[0], v0[1]); xw.y = cvt_pk_bf16(v0[2], v0[3]); xw.z = cvt_pk_bf16(v1[0], v1[1]); xw.w = cvt_pk_bf16(v1[2], v1[3]); *(u32x4*)(C + off + bj * HALF) = xw; }
;                     const f32x4 h0 = v0 * gv[bj][0], h1 = v1 * gv[bj][1];
;                     u32x2 w; w.x = cvt_pk4_fp8(h0[0], h0[1], h0[2], h0[3]); w.y = cvt_pk4_fp8(h1[0], h1[1], h1[2], h1[3]);
;                     *(u32x2*)(H2 + off + bj * HALF) = w; } }
.LBB0_921:
	s_lshl_b32 s36, s52, 8
	v_mbcnt_lo_u32_b32 v96, -1, 0
	v_mbcnt_hi_u32_b32 v96, -1, v96
	s_add_i32 s36, s36, s34
	s_lshl_b32 s35, s35, 8
	v_ashrrev_i32_e32 v97, 1, v96
	s_or_b32 s35, s35, s84
	v_and_b32_e32 v97, -8, v97
	v_and_or_b32 v144, v96, 15, s36
	v_add_u32_e32 v148, s35, v97
	v_ashrrev_i32_e32 v145, 31, v144
	v_ashrrev_i32_e32 v149, 31, v148
	v_lshlrev_b64 v[96:97], 11, v[144:145]
	v_lshl_add_u64 v[146:147], v[96:97], 0, v[148:149]
	v_lshl_add_u64 v[168:169], v[146:147], 2, s[6:7]
	global_load_dwordx4 v[160:163], v[168:169], off
	global_load_dwordx4 v[164:167], v[168:169], off offset:16
	v_lshl_add_u64 v[100:101], v[148:149], 2, s[12:13]
	global_load_dwordx4 v[116:119], v[100:101], off
	global_load_dwordx4 v[112:115], v[100:101], off offset:16
	global_load_dwordx4 v[96:99], v[100:101], off offset:528
	s_nop 0
	global_load_dwordx4 v[100:103], v[100:101], off offset:512
	v_lshlrev_b32_e32 v248, 2, v146
	global_load_dwordx4 v[176:179], v248, s[6:7] offset:512
	global_load_dwordx4 v[180:183], v248, s[6:7] offset:528
	v_add_u32_e32 v249, 0x20000, v248
	global_load_dwordx4 v[184:187], v249, s[6:7]
	global_load_dwordx4 v[188:191], v249, s[6:7] offset:16
	v_add_u32_e32 v249, 0x20000, v248
	global_load_dwordx4 v[192:195], v249, s[6:7] offset:512
	global_load_dwordx4 v[196:199], v249, s[6:7] offset:528
	v_add_u32_e32 v249, 0x40000, v248
	global_load_dwordx4 v[200:203], v249, s[6:7]
	global_load_dwordx4 v[204:207], v249, s[6:7] offset:16
	v_add_u32_e32 v249, 0x40000, v248
	global_load_dwordx4 v[208:211], v249, s[6:7] offset:512
	global_load_dwordx4 v[212:215], v249, s[6:7] offset:528
	v_add_u32_e32 v249, 0x60000, v248
	global_load_dwordx4 v[216:219], v249, s[6:7]
	global_load_dwordx4 v[220:223], v249, s[6:7] offset:16
	v_add_u32_e32 v249, 0x60000, v248
	global_load_dwordx4 v[224:227], v249, s[6:7] offset:512
	global_load_dwordx4 v[228:231], v249, s[6:7] offset:528
	v_add_u32_e32 v249, 0x100000, v248
	global_load_dwordx4 v[232:235], v249, s[6:7]
	global_load_dwordx4 v[236:239], v249, s[6:7] offset:16
	v_add_u32_e32 v249, 0x100000, v248
	global_load_dwordx4 v[240:243], v249, s[6:7] offset:512
	global_load_dwordx4 v[244:247], v249, s[6:7] offset:528
	v_lshl_add_u64 v[172:173], v[146:147], 1, s[14:15]
	v_lshl_add_u64 v[174:175], s[10:11], 0, v[146:147]
	s_andn2_b64 vcc, exec, s[50:51]
	s_mov_b64 s[50:51], -1
	s_waitcnt vmcnt(23)
	v_pk_add_f32 v[140:141], v[140:141], v[160:161]
	s_waitcnt vmcnt(22)
	v_pk_add_f32 v[160:161], v[138:139], v[166:167]
	v_pk_add_f32 v[138:139], v[136:137], v[164:165]
	v_pk_add_f32 v[142:143], v[142:143], v[162:163]
	v_cvt_pk_bf16_f32 v136, v140, v141
	s_waitcnt vmcnt(21)
	v_pk_mul_f32 v[140:141], v[116:117], v[140:141]
	s_waitcnt vmcnt(20)
	v_pk_mul_f32 v[162:163], v[112:113], v[138:139]
	v_cvt_pk_fp8_f32 v170, v140, v141
	v_cvt_pk_fp8_f32 v171, v162, v163
	v_cvt_pk_bf16_f32 v137, v142, v143
	v_pk_mul_f32 v[140:141], v[118:119], v[142:143]
	v_pk_mul_f32 v[142:143], v[114:115], v[160:161]
	v_cvt_pk_fp8_f32 v170, v140, v141 op_sel:[0,0,1]
	v_cvt_pk_fp8_f32 v171, v142, v143 op_sel:[0,0,1]
	v_cvt_pk_bf16_f32 v138, v138, v139
	v_cvt_pk_bf16_f32 v139, v160, v161
	global_store_dwordx4 v[172:173], v[136:139], off
	global_store_dwordx2 v[174:175], v[170:171], off
	v_or_b32_e32 v162, 16, v144
	v_ashrrev_i32_e32 v163, 31, v162
	v_lshlrev_b64 v[162:163], 11, v[162:163]
	v_lshl_add_u64 v[162:163], v[162:163], 0, v[148:149]
	v_lshl_add_u64 v[164:165], v[162:163], 2, s[6:7]
	s_waitcnt vmcnt(18)
	v_pk_add_f32 v[132:133], v[132:133], v[176:177]
	v_pk_add_f32 v[136:137], v[130:131], v[182:183]
	v_pk_add_f32 v[130:131], v[128:129], v[180:181]
	v_pk_add_f32 v[134:135], v[134:135], v[178:179]
	v_add_u32_e32 v249, 0x120000, v248
	global_load_dwordx4 v[176:179], v249, s[6:7]
	global_load_dwordx4 v[180:183], v249, s[6:7] offset:16
	v_cvt_pk_bf16_f32 v128, v132, v133
	v_pk_mul_f32 v[132:133], v[100:101], v[132:133]
	v_pk_mul_f32 v[138:139], v[96:97], v[130:131]
	v_cvt_pk_fp8_f32 v160, v132, v133
	v_cvt_pk_fp8_f32 v161, v138, v139
	v_cvt_pk_bf16_f32 v129, v134, v135
	v_pk_mul_f32 v[132:133], v[102:103], v[134:135]
	v_pk_mul_f32 v[134:135], v[98:99], v[136:137]
	v_cvt_pk_fp8_f32 v160, v132, v133 op_sel:[0,0,1]
	v_cvt_pk_fp8_f32 v161, v134, v135 op_sel:[0,0,1]
	v_cvt_pk_bf16_f32 v130, v130, v131
	v_cvt_pk_bf16_f32 v131, v136, v137
	global_store_dwordx4 v[172:173], v[128:131], off offset:256
	global_store_dwordx2 v[174:175], v[160:161], off offset:128
	v_lshl_add_u64 v[138:139], v[162:163], 1, s[14:15]
	v_lshl_add_u64 v[140:141], s[10:11], 0, v[162:163]
	s_waitcnt vmcnt(20)
	v_pk_add_f32 v[124:125], v[124:125], v[184:185]
	v_pk_add_f32 v[128:129], v[122:123], v[190:191]
	v_pk_add_f32 v[122:123], v[120:121], v[188:189]
	v_pk_add_f32 v[126:127], v[126:127], v[186:187]
	v_add_u32_e32 v249, 0x120000, v248
	global_load_dwordx4 v[184:187], v249, s[6:7] offset:512
	global_load_dwordx4 v[188:191], v249, s[6:7] offset:528
	v_cvt_pk_bf16_f32 v120, v124, v125
	v_pk_mul_f32 v[124:125], v[116:117], v[124:125]
	v_pk_mul_f32 v[130:131], v[112:113], v[122:123]
	v_cvt_pk_fp8_f32 v136, v124, v125
	v_cvt_pk_fp8_f32 v137, v130, v131
	v_cvt_pk_bf16_f32 v121, v126, v127
	v_pk_mul_f32 v[124:125], v[118:119], v[126:127]
	v_pk_mul_f32 v[126:127], v[114:115], v[128:129]
	v_cvt_pk_fp8_f32 v136, v124, v125 op_sel:[0,0,1]
	v_cvt_pk_fp8_f32 v137, v126, v127 op_sel:[0,0,1]
	v_cvt_pk_bf16_f32 v122, v122, v123
	v_cvt_pk_bf16_f32 v123, v128, v129
	global_store_dwordx4 v[138:139], v[120:123], off
	global_store_dwordx2 v[140:141], v[136:137], off
	v_or_b32_e32 v130, 32, v144
	v_ashrrev_i32_e32 v131, 31, v130
	v_lshlrev_b64 v[130:131], 11, v[130:131]
	v_lshl_add_u64 v[130:131], v[130:131], 0, v[148:149]
	v_lshl_add_u64 v[132:133], v[130:131], 2, s[6:7]
	s_waitcnt vmcnt(22)
; __device__ __forceinline__ unsigned cvt_pk_bf16(float lo, float hi) { unsigned r; asm volatile("v_cvt_pk_bf16_f32 %0, %1, %2" : "=v"(r) : "v"(lo), "v"(hi)); return r; }
; __device__ __forceinline__ unsigned cvt_pk4_fp8(float a, float b, float c, float d) { int w; asm("" : "=v"(w));     w = __builtin_amdgcn_cvt_pk_fp8_f32(a, b, w, false); w = __builtin_amdgcn_cvt_pk_fp8_f32(c, d, w, true); return (unsigned)w; }
;     __device__ __forceinline__ void operator()(const f32x4 (&acc)[2][2][4][2], const Unit& u, int wr, int wc, int fr, int fq) const {
;     ...
;         for (int ai = 0; ai < 2; ++ai)
; #pragma unroll
;             for (int m = 0; m < 4; ++m) { const size_t off = (size_t)(row0 + ai * HALF + m * 16) * DM + col0;
; #pragma unroll
;                 for (int bj = 0; bj < 2; ++bj) { const f32x4 v0 = *(const f32x4*)(base + off + bj * HALF) + acc[ai][bj][m][0], v1 = *(const f32x4*)(base + off + bj * HALF + 4) + acc[ai][bj][m][1];
;                     { u32x4 xw; xw.x = cvt_pk_bf16(v0[0], v0[1]); xw.y = cvt_pk_bf16(v0[2], v0[3]); xw.z = cvt_pk_bf16(v1[0], v1[1]); xw.w = cvt_pk_bf16(v1[2], v1[3]); *(u32x4*)(C + off + bj * HALF) = xw; }
;                     const f32x4 h0 = v0 * gv[bj][0], h1 = v1 * gv[bj][1];
;                     u32x2 w; w.x = cvt_pk4_fp8(h0[0], h0[1], h0[2], h0[3]); w.y = cvt_pk4_fp8(h1[0], h1[1], h1[2], h1[3]);
;                     *(u32x2*)(H2 + off + bj * HALF) = w; } }
	v_pk_add_f32 v[108:109], v[108:109], v[192:193]
	v_pk_add_f32 v[120:121], v[106:107], v[198:199]
	v_pk_add_f32 v[106:107], v[104:105], v[196:197]
	v_pk_add_f32 v[110:111], v[110:111], v[194:195]
	v_add_u32_e32 v249, 0x140000, v248
	global_load_dwordx4 v[192:195], v249, s[6:7]
	global_load_dwordx4 v[196:199], v249, s[6:7] offset:16
	v_cvt_pk_bf16_f32 v104, v108, v109
	v_pk_mul_f32 v[108:109], v[100:101], v[108:109]
	v_pk_mul_f32 v[122:123], v[96:97], v[106:107]
	v_cvt_pk_fp8_f32 v128, v108, v109
	v_cvt_pk_fp8_f32 v129, v122, v123
	v_cvt_pk_bf16_f32 v105, v110, v111
	v_pk_mul_f32 v[108:109], v[102:103], v[110:111]
	v_pk_mul_f32 v[110:111], v[98:99], v[120:121]
	v_cvt_pk_fp8_f32 v128, v108, v109 op_sel:[0,0,1]
	v_cvt_pk_fp8_f32 v129, v110, v111 op_sel:[0,0,1]
	v_cvt_pk_bf16_f32 v106, v106, v107
	v_cvt_pk_bf16_f32 v107, v120, v121
	global_store_dwordx4 v[138:139], v[104:107], off offset:256
	global_store_dwordx2 v[140:141], v[128:129], off offset:128
	v_lshl_add_u64 v[122:123], v[130:131], 1, s[14:15]
	v_lshl_add_u64 v[124:125], s[10:11], 0, v[130:131]
	s_waitcnt vmcnt(24)
	v_pk_add_f32 v[92:93], v[92:93], v[200:201]
	v_pk_add_f32 v[104:105], v[90:91], v[206:207]
	v_pk_add_f32 v[90:91], v[88:89], v[204:205]
	v_pk_add_f32 v[94:95], v[94:95], v[202:203]
	v_add_u32_e32 v249, 0x140000, v248
	global_load_dwordx4 v[200:203], v249, s[6:7] offset:512
	global_load_dwordx4 v[204:207], v249, s[6:7] offset:528
	v_cvt_pk_bf16_f32 v88, v92, v93
	v_pk_mul_f32 v[92:93], v[116:117], v[92:93]
	v_pk_mul_f32 v[106:107], v[112:113], v[90:91]
	v_cvt_pk_fp8_f32 v120, v92, v93
	v_cvt_pk_fp8_f32 v121, v106, v107
	v_cvt_pk_bf16_f32 v89, v94, v95
	v_pk_mul_f32 v[92:93], v[118:119], v[94:95]
	v_pk_mul_f32 v[94:95], v[114:115], v[104:105]
	v_cvt_pk_fp8_f32 v120, v92, v93 op_sel:[0,0,1]
	v_cvt_pk_fp8_f32 v121, v94, v95 op_sel:[0,0,1]
	v_cvt_pk_bf16_f32 v90, v90, v91
	v_cvt_pk_bf16_f32 v91, v104, v105
	global_store_dwordx4 v[122:123], v[88:91], off
	global_store_dwordx2 v[124:125], v[120:121], off
	v_or_b32_e32 v106, 48, v144
	v_ashrrev_i32_e32 v107, 31, v106
	v_lshlrev_b64 v[106:107], 11, v[106:107]
	v_lshl_add_u64 v[106:107], v[106:107], 0, v[148:149]
	v_lshl_add_u64 v[108:109], v[106:107], 2, s[6:7]
	s_waitcnt vmcnt(26)
	v_pk_add_f32 v[84:85], v[84:85], v[208:209]
	v_pk_add_f32 v[88:89], v[82:83], v[214:215]
	v_pk_add_f32 v[82:83], v[80:81], v[212:213]
	v_pk_add_f32 v[86:87], v[86:87], v[210:211]
	v_add_u32_e32 v249, 0x160000, v248
	global_load_dwordx4 v[208:211], v249, s[6:7]
	global_load_dwordx4 v[212:215], v249, s[6:7] offset:16
	v_cvt_pk_bf16_f32 v80, v84, v85
	v_pk_mul_f32 v[84:85], v[100:101], v[84:85]
	v_pk_mul_f32 v[90:91], v[96:97], v[82:83]
	v_cvt_pk_fp8_f32 v104, v84, v85
	v_cvt_pk_fp8_f32 v105, v90, v91
	v_cvt_pk_bf16_f32 v81, v86, v87
	v_pk_mul_f32 v[84:85], v[102:103], v[86:87]
	v_pk_mul_f32 v[86:87], v[98:99], v[88:89]
	v_cvt_pk_fp8_f32 v104, v84, v85 op_sel:[0,0,1]
	v_cvt_pk_fp8_f32 v105, v86, v87 op_sel:[0,0,1]
	v_cvt_pk_bf16_f32 v82, v82, v83
	v_cvt_pk_bf16_f32 v83, v88, v89
	global_store_dwordx4 v[122:123], v[80:83], off offset:256
	global_store_dwordx2 v[124:125], v[104:105], off offset:128
	v_lshl_add_u64 v[90:91], v[106:107], 1, s[14:15]
	v_lshl_add_u64 v[92:93], s[10:11], 0, v[106:107]
	s_waitcnt vmcnt(28)
	v_pk_add_f32 v[76:77], v[76:77], v[216:217]
	v_pk_add_f32 v[80:81], v[74:75], v[222:223]
	v_pk_add_f32 v[74:75], v[72:73], v[220:221]
	v_pk_add_f32 v[78:79], v[78:79], v[218:219]
	v_add_u32_e32 v249, 0x160000, v248
	global_load_dwordx4 v[216:219], v249, s[6:7] offset:512
	global_load_dwordx4 v[220:223], v249, s[6:7] offset:528
	v_cvt_pk_bf16_f32 v72, v76, v77
	v_pk_mul_f32 v[76:77], v[116:117], v[76:77]
	v_pk_mul_f32 v[82:83], v[112:113], v[74:75]
	v_cvt_pk_fp8_f32 v88, v76, v77
	v_cvt_pk_fp8_f32 v89, v82, v83
	v_cvt_pk_bf16_f32 v73, v78, v79
	v_pk_mul_f32 v[76:77], v[118:119], v[78:79]
	v_pk_mul_f32 v[78:79], v[114:115], v[80:81]
	v_cvt_pk_fp8_f32 v88, v76, v77 op_sel:[0,0,1]
	v_cvt_pk_fp8_f32 v89, v78, v79 op_sel:[0,0,1]
	v_cvt_pk_bf16_f32 v74, v74, v75
	v_cvt_pk_bf16_f32 v75, v80, v81
	global_store_dwordx4 v[90:91], v[72:75], off
	global_store_dwordx2 v[92:93], v[88:89], off
	v_lshl_add_u64 v[82:83], v[146:147], 0, s[20:21]
	v_lshl_add_u64 v[84:85], v[82:83], 2, s[6:7]
	s_waitcnt vmcnt(30)
	v_pk_add_f32 v[68:69], v[68:69], v[224:225]
	v_pk_add_f32 v[72:73], v[66:67], v[230:231]
	v_pk_add_f32 v[66:67], v[64:65], v[228:229]
	v_pk_add_f32 v[70:71], v[70:71], v[226:227]
	v_cvt_pk_bf16_f32 v64, v68, v69
	v_pk_mul_f32 v[68:69], v[100:101], v[68:69]
	v_pk_mul_f32 v[74:75], v[96:97], v[66:67]
	v_cvt_pk_fp8_f32 v80, v68, v69
	v_cvt_pk_fp8_f32 v81, v74, v75
	v_cvt_pk_bf16_f32 v65, v70, v71
	v_pk_mul_f32 v[68:69], v[102:103], v[70:71]
	v_pk_mul_f32 v[70:71], v[98:99], v[72:73]
	v_cvt_pk_fp8_f32 v80, v68, v69 op_sel:[0,0,1]
	v_cvt_pk_fp8_f32 v81, v70, v71 op_sel:[0,0,1]
	v_cvt_pk_bf16_f32 v66, v66, v67
	v_cvt_pk_bf16_f32 v67, v72, v73
	global_store_dwordx4 v[90:91], v[64:67], off offset:256
	global_store_dwordx2 v[92:93], v[80:81], off offset:128
	v_lshl_add_u64 v[74:75], v[82:83], 1, s[14:15]
	v_lshl_add_u64 v[76:77], s[10:11], 0, v[82:83]
	s_waitcnt vmcnt(30)
	v_pk_add_f32 v[60:61], v[60:61], v[232:233]
	v_pk_add_f32 v[64:65], v[58:59], v[238:239]
	v_pk_add_f32 v[58:59], v[56:57], v[236:237]
	v_pk_add_f32 v[62:63], v[62:63], v[234:235]
	v_cvt_pk_bf16_f32 v56, v60, v61
	v_pk_mul_f32 v[60:61], v[116:117], v[60:61]
	v_pk_mul_f32 v[66:67], v[112:113], v[58:59]
	v_cvt_pk_fp8_f32 v72, v60, v61
	v_cvt_pk_fp8_f32 v73, v66, v67
	v_cvt_pk_bf16_f32 v57, v62, v63
	v_pk_mul_f32 v[60:61], v[118:119], v[62:63]
	v_pk_mul_f32 v[62:63], v[114:115], v[64:65]
	v_cvt_pk_fp8_f32 v72, v60, v61 op_sel:[0,0,1]
	v_cvt_pk_fp8_f32 v73, v62, v63 op_sel:[0,0,1]
	v_cvt_pk_bf16_f32 v58, v58, v59
	v_cvt_pk_bf16_f32 v59, v64, v65
	global_store_dwordx4 v[74:75], v[56:59], off
	global_store_dwordx2 v[76:77], v[72:73], off
	v_lshl_add_u64 v[66:67], v[146:147], 0, s[22:23]
	v_lshl_add_u64 v[68:69], v[66:67], 2, s[6:7]
	s_waitcnt vmcnt(30)
; __device__ __forceinline__ unsigned cvt_pk_bf16(float lo, float hi) { unsigned r; asm volatile("v_cvt_pk_bf16_f32 %0, %1, %2" : "=v"(r) : "v"(lo), "v"(hi)); return r; }
; __device__ __forceinline__ unsigned cvt_pk4_fp8(float a, float b, float c, float d) { int w; asm("" : "=v"(w));     w = __builtin_amdgcn_cvt_pk_fp8_f32(a, b, w, false); w = __builtin_amdgcn_cvt_pk_fp8_f32(c, d, w, true); return (unsigned)w; }
;     __device__ __forceinline__ void operator()(const f32x4 (&acc)[2][2][4][2], const Unit& u, int wr, int wc, int fr, int fq) const {
;     ...
;         for (int ai = 0; ai < 2; ++ai)
; #pragma unroll
;             for (int m = 0; m < 4; ++m) { const size_t off = (size_t)(row0 + ai * HALF + m * 16) * DM + col0;
; #pragma unroll
;                 for (int bj = 0; bj < 2; ++bj) { const f32x4 v0 = *(const f32x4*)(base + off + bj * HALF) + acc[ai][bj][m][0], v1 = *(const f32x4*)(base + off + bj * HALF + 4) + acc[ai][bj][m][1];
;                     { u32x4 xw; xw.x = cvt_pk_bf16(v0[0], v0[1]); xw.y = cvt_pk_bf16(v0[2], v0[3]); xw.z = cvt_pk_bf16(v1[0], v1[1]); xw.w = cvt_pk_bf16(v1[2], v1[3]); *(u32x4*)(C + off + bj * HALF) = xw; }
;                     const f32x4 h0 = v0 * gv[bj][0], h1 = v1 * gv[bj][1];
;                     u32x2 w; w.x = cvt_pk4_fp8(h0[0], h0[1], h0[2], h0[3]); w.y = cvt_pk4_fp8(h1[0], h1[1], h1[2], h1[3]);
;                     *(u32x2*)(H2 + off + bj * HALF) = w; } }
	v_pk_add_f32 v[52:53], v[52:53], v[240:241]
	v_pk_add_f32 v[56:57], v[50:51], v[246:247]
	v_pk_add_f32 v[50:51], v[48:49], v[244:245]
	v_pk_add_f32 v[54:55], v[54:55], v[242:243]
	v_cvt_pk_bf16_f32 v48, v52, v53
	v_pk_mul_f32 v[52:53], v[100:101], v[52:53]
	v_pk_mul_f32 v[58:59], v[96:97], v[50:51]
	v_cvt_pk_fp8_f32 v64, v52, v53
	v_cvt_pk_fp8_f32 v65, v58, v59
	v_cvt_pk_bf16_f32 v49, v54, v55
	v_pk_mul_f32 v[52:53], v[102:103], v[54:55]
	v_pk_mul_f32 v[54:55], v[98:99], v[56:57]
	v_cvt_pk_fp8_f32 v64, v52, v53 op_sel:[0,0,1]
	v_cvt_pk_fp8_f32 v65, v54, v55 op_sel:[0,0,1]
	v_cvt_pk_bf16_f32 v50, v50, v51
	v_cvt_pk_bf16_f32 v51, v56, v57
	global_store_dwordx4 v[74:75], v[48:51], off offset:256
	global_store_dwordx2 v[76:77], v[64:65], off offset:128
	v_lshl_add_u64 v[58:59], v[66:67], 1, s[14:15]
	v_lshl_add_u64 v[60:61], s[10:11], 0, v[66:67]
	s_waitcnt vmcnt(28)
	v_pk_add_f32 v[44:45], v[44:45], v[176:177]
	v_pk_add_f32 v[48:49], v[42:43], v[182:183]
	v_pk_add_f32 v[42:43], v[40:41], v[180:181]
	v_pk_add_f32 v[46:47], v[46:47], v[178:179]
	v_cvt_pk_bf16_f32 v40, v44, v45
	v_pk_mul_f32 v[44:45], v[116:117], v[44:45]
	v_pk_mul_f32 v[50:51], v[112:113], v[42:43]
	v_cvt_pk_fp8_f32 v56, v44, v45
	v_cvt_pk_fp8_f32 v57, v50, v51
	v_cvt_pk_bf16_f32 v41, v46, v47
	v_pk_mul_f32 v[44:45], v[118:119], v[46:47]
	v_pk_mul_f32 v[46:47], v[114:115], v[48:49]
	v_cvt_pk_fp8_f32 v56, v44, v45 op_sel:[0,0,1]
	v_cvt_pk_fp8_f32 v57, v46, v47 op_sel:[0,0,1]
	v_cvt_pk_bf16_f32 v42, v42, v43
	v_cvt_pk_bf16_f32 v43, v48, v49
	global_store_dwordx4 v[58:59], v[40:43], off
	global_store_dwordx2 v[60:61], v[56:57], off
	v_lshl_add_u64 v[50:51], v[146:147], 0, s[24:25]
	v_lshl_add_u64 v[52:53], v[50:51], 2, s[6:7]
	s_waitcnt vmcnt(26)
	v_pk_add_f32 v[36:37], v[36:37], v[184:185]
	v_pk_add_f32 v[40:41], v[34:35], v[190:191]
	v_pk_add_f32 v[34:35], v[32:33], v[188:189]
	v_pk_add_f32 v[38:39], v[38:39], v[186:187]
	v_cvt_pk_bf16_f32 v32, v36, v37
	v_pk_mul_f32 v[36:37], v[100:101], v[36:37]
	v_pk_mul_f32 v[42:43], v[96:97], v[34:35]
	v_cvt_pk_fp8_f32 v48, v36, v37
	v_cvt_pk_fp8_f32 v49, v42, v43
	v_cvt_pk_bf16_f32 v33, v38, v39
	v_pk_mul_f32 v[36:37], v[102:103], v[38:39]
	v_pk_mul_f32 v[38:39], v[98:99], v[40:41]
	v_cvt_pk_fp8_f32 v48, v36, v37 op_sel:[0,0,1]
	v_cvt_pk_fp8_f32 v49, v38, v39 op_sel:[0,0,1]
	v_cvt_pk_bf16_f32 v34, v34, v35
	v_cvt_pk_bf16_f32 v35, v40, v41
	global_store_dwordx4 v[58:59], v[32:35], off offset:256
	global_store_dwordx2 v[60:61], v[48:49], off offset:128
	v_lshl_add_u64 v[42:43], v[50:51], 1, s[14:15]
	v_lshl_add_u64 v[44:45], s[10:11], 0, v[50:51]
	s_waitcnt vmcnt(24)
	v_pk_add_f32 v[28:29], v[28:29], v[192:193]
	v_pk_add_f32 v[32:33], v[26:27], v[198:199]
	v_pk_add_f32 v[26:27], v[24:25], v[196:197]
	v_pk_add_f32 v[30:31], v[30:31], v[194:195]
	v_cvt_pk_bf16_f32 v24, v28, v29
	v_pk_mul_f32 v[28:29], v[116:117], v[28:29]
	v_pk_mul_f32 v[34:35], v[112:113], v[26:27]
	v_cvt_pk_fp8_f32 v40, v28, v29
	v_cvt_pk_fp8_f32 v41, v34, v35
	v_cvt_pk_bf16_f32 v25, v30, v31
	v_pk_mul_f32 v[28:29], v[118:119], v[30:31]
	v_pk_mul_f32 v[30:31], v[114:115], v[32:33]
	v_cvt_pk_fp8_f32 v40, v28, v29 op_sel:[0,0,1]
	v_cvt_pk_fp8_f32 v41, v30, v31 op_sel:[0,0,1]
	v_cvt_pk_bf16_f32 v26, v26, v27
	v_cvt_pk_bf16_f32 v27, v32, v33
	global_store_dwordx4 v[42:43], v[24:27], off
	global_store_dwordx2 v[44:45], v[40:41], off
	v_lshl_add_u64 v[34:35], v[146:147], 0, s[26:27]
	v_lshl_add_u64 v[36:37], v[34:35], 2, s[6:7]
	s_waitcnt vmcnt(22)
	v_pk_add_f32 v[20:21], v[20:21], v[200:201]
	v_pk_add_f32 v[24:25], v[18:19], v[206:207]
	v_pk_add_f32 v[18:19], v[16:17], v[204:205]
	v_pk_add_f32 v[22:23], v[22:23], v[202:203]
	v_cvt_pk_bf16_f32 v16, v20, v21
	v_pk_mul_f32 v[20:21], v[100:101], v[20:21]
	v_pk_mul_f32 v[26:27], v[96:97], v[18:19]
	v_cvt_pk_fp8_f32 v32, v20, v21
	v_cvt_pk_fp8_f32 v33, v26, v27
	v_cvt_pk_bf16_f32 v17, v22, v23
	v_pk_mul_f32 v[20:21], v[102:103], v[22:23]
	v_pk_mul_f32 v[22:23], v[98:99], v[24:25]
	v_cvt_pk_fp8_f32 v32, v20, v21 op_sel:[0,0,1]
	v_cvt_pk_fp8_f32 v33, v22, v23 op_sel:[0,0,1]
	v_cvt_pk_bf16_f32 v18, v18, v19
	v_cvt_pk_bf16_f32 v19, v24, v25
	global_store_dwordx4 v[42:43], v[16:19], off offset:256
	global_store_dwordx2 v[44:45], v[32:33], off offset:128
	v_lshl_add_u64 v[26:27], v[34:35], 1, s[14:15]
	v_lshl_add_u64 v[28:29], s[10:11], 0, v[34:35]
	s_waitcnt vmcnt(20)
	v_pk_add_f32 v[12:13], v[12:13], v[208:209]
	v_pk_add_f32 v[16:17], v[10:11], v[214:215]
	v_pk_add_f32 v[10:11], v[8:9], v[212:213]
	v_pk_add_f32 v[14:15], v[14:15], v[210:211]
	v_cvt_pk_bf16_f32 v8, v12, v13
	v_pk_mul_f32 v[12:13], v[116:117], v[12:13]
	v_pk_mul_f32 v[18:19], v[112:113], v[10:11]
	v_cvt_pk_fp8_f32 v24, v12, v13
	v_cvt_pk_fp8_f32 v25, v18, v19
	v_cvt_pk_bf16_f32 v9, v14, v15
	v_pk_mul_f32 v[12:13], v[118:119], v[14:15]
	v_pk_mul_f32 v[14:15], v[114:115], v[16:17]
	v_cvt_pk_fp8_f32 v24, v12, v13 op_sel:[0,0,1]
	v_cvt_pk_fp8_f32 v25, v14, v15 op_sel:[0,0,1]
	v_cvt_pk_bf16_f32 v10, v10, v11
	v_cvt_pk_bf16_f32 v11, v16, v17
	global_store_dwordx4 v[26:27], v[8:11], off
	global_store_dwordx2 v[28:29], v[24:25], off
	s_waitcnt vmcnt(18)
	v_pk_add_f32 v[4:5], v[4:5], v[216:217]
	v_pk_add_f32 v[8:9], v[2:3], v[222:223]
	v_pk_add_f32 v[2:3], v[0:1], v[220:221]
	v_pk_add_f32 v[6:7], v[6:7], v[218:219]
	v_cvt_pk_bf16_f32 v0, v4, v5
	v_pk_mul_f32 v[4:5], v[100:101], v[4:5]
	v_pk_mul_f32 v[10:11], v[96:97], v[2:3]
	v_cvt_pk_fp8_f32 v144, v4, v5
	v_cvt_pk_fp8_f32 v145, v10, v11
	v_cvt_pk_bf16_f32 v1, v6, v7
	v_pk_mul_f32 v[4:5], v[102:103], v[6:7]
	v_pk_mul_f32 v[6:7], v[98:99], v[8:9]
	v_cvt_pk_fp8_f32 v144, v4, v5 op_sel:[0,0,1]
	v_cvt_pk_fp8_f32 v145, v6, v7 op_sel:[0,0,1]
	v_cvt_pk_bf16_f32 v2, v2, v3
	v_cvt_pk_bf16_f32 v3, v8, v9
	global_store_dwordx4 v[26:27], v[0:3], off offset:256
	global_store_dwordx2 v[28:29], v[144:145], off offset:128
	s_cbranch_vccnz .LBB0_910
	s_andn2_b64 vcc, exec, s[16:17]
	s_cbranch_vccnz .LBB0_909
	s_barrier
	s_branch .LBB0_909
